# split-barrier posts moved inside the following stage (no extra drain/s_barrier at the junction): scan pass1 posted after Fourier stage 0's first barrier, stage C after the correction stage's first bar
# speedup vs baseline: 1.0325x; 1.0014x over previous
.LBB0_368:
	v_readfirstlane_b32 s99, v186
	s_nop 0
	s_cmp_lg_u32 s99, 0
	s_cselect_b32 s99, 2, 0
	v_mov_b32_e32 v0, v186
	s_and_b64 vcc, exec, s[6:7]
	s_cbranch_vccnz .LBB0_373
	v_lshlrev_b32_e32 v2, 4, v0
	v_and_b32_e32 v2, 0xf0, v2
	v_mov_b32_e32 v3, 0
	s_waitcnt lgkmcnt(0)
	v_lshl_add_u64 v[4:5], s[2:3], 0, v[2:3]
	s_mov_b64 s[0:1], 0xa7b000
	v_bfe_u32 v9, v0, 4, 2
	v_lshl_add_u64 v[32:33], v[4:5], 0, s[0:1]
	v_ashrrev_i32_e32 v4, 2, v0
	v_and_b32_e32 v1, 15, v0
	v_and_b32_e32 v11, -16, v4
	v_bfi_b32 v38, -16, v4, v0
	v_lshlrev_b32_e32 v4, 4, v9
	v_mov_b32_e32 v5, v3
	v_lshl_add_u64 v[6:7], s[2:3], 0, v[4:5]
	v_add_u32_e32 v5, 0, v2
	v_lshlrev_b32_e32 v2, 2, v1
	v_lshl_add_u64 v[2:3], s[2:3], 0, v[2:3]
	s_mov_b64 s[2:3], 0x112f3000
	v_lshl_add_u64 v[36:37], v[2:3], 0, s[2:3]
	v_lshlrev_b32_e32 v3, 2, v0
	v_ashrrev_i32_e32 v2, 11, v0
	v_and_b32_e32 v3, 0x1fc0, v3
	s_mov_b64 s[0:1], 0x1a7b000
	v_add_u32_e32 v41, v3, v2
	v_add_u32_e32 v2, 0x200, v0
	v_bfe_u32 v10, v0, 4, 4
	v_lshl_add_u64 v[34:35], v[6:7], 0, s[0:1]
	v_ashrrev_i32_e32 v6, 11, v2
	v_lshrrev_b32_e32 v2, 4, v2
	s_movk_i32 s0, 0x70
	v_and_or_b32 v7, v2, s0, v10
	v_lshl_add_u32 v42, v7, 6, v6
	v_add_u32_e32 v6, 0x400, v0
	v_ashrrev_i32_e32 v7, 11, v6
	v_lshrrev_b32_e32 v6, 4, v6
	v_lshl_or_b32 v40, v9, 2, v11
	v_and_or_b32 v9, v6, s0, v10
	v_lshl_add_u32 v43, v9, 6, v7
	v_add_u32_e32 v7, 0x600, v0
	v_ashrrev_i32_e32 v9, 11, v7
	v_lshrrev_b32_e32 v7, 4, v7
	v_and_or_b32 v11, v7, s0, v10
	v_lshl_add_u32 v44, v11, 6, v9
	v_add_u32_e32 v9, 0x800, v0
	v_ashrrev_i32_e32 v11, 11, v9
	v_add_u32_e32 v45, v3, v11
	v_add_u32_e32 v3, 0xa00, v0
	v_ashrrev_i32_e32 v11, 11, v3
	v_lshrrev_b32_e32 v3, 4, v3
	v_and_or_b32 v12, v3, s0, v10
	v_lshl_add_u32 v46, v12, 6, v11
	v_add_u32_e32 v11, 0xc00, v0
	v_ashrrev_i32_e32 v12, 11, v11
	v_lshrrev_b32_e32 v11, 4, v11
	v_lshrrev_b32_e32 v8, 4, v0
	v_and_or_b32 v13, v11, s0, v10
	v_add_u32_e32 v0, 0xe00, v0
	v_lshl_add_u32 v47, v13, 6, v12
	v_ashrrev_i32_e32 v12, 11, v0
	v_lshrrev_b32_e32 v0, 4, v0
	v_and_or_b32 v10, v0, s0, v10
	s_movk_i32 s0, 0x110
	v_lshrrev_b32_e32 v9, 4, v9
	v_lshl_add_u32 v48, v10, 6, v12
	v_mul_lo_u32 v8, v8, s0
	v_mul_lo_u32 v2, v2, s0
	v_mul_lo_u32 v6, v6, s0
	v_mul_lo_u32 v7, v7, s0
	v_mul_lo_u32 v9, v9, s0
	v_mul_lo_u32 v3, v3, s0
	v_mul_lo_u32 v10, v11, s0
	v_mul_lo_u32 v0, v0, s0
	v_mul_u32_u24_e32 v1, 0x110, v1
	v_readlane_b32 s2, v235, 16
	v_add_u32_e32 v39, 0x80, v38
	s_mov_b32 s1, 0
	v_add3_u32 v49, v1, v4, 0
	v_add_u32_e32 v50, v5, v8
	v_add_u32_e32 v51, v5, v2
	v_add_u32_e32 v52, v5, v6
	v_add_u32_e32 v53, v5, v7
	v_add_u32_e32 v54, v5, v9
	v_add_u32_e32 v55, v5, v3
	v_add_u32_e32 v56, v5, v10
	v_add_u32_e32 v57, v5, v0
	s_mov_b32 s8, s2
	v_readlane_b32 s3, v235, 17
.LBB0_370:
	s_bfe_u32 s9, s8, 0x10005
	s_lshl_b32 s2, s8, 1
	s_and_b32 s10, s2, 62
	s_lshl_b32 s2, s9, 13
	s_ashr_i32 s0, s8, 6
	s_or_b32 s11, s2, s10
	s_lshl_b32 s2, s0, 7
	v_add_u32_e32 v2, s11, v41
	v_add_u32_e32 v4, s11, v42
	s_ashr_i32 s3, s2, 31
	v_ashrrev_i32_e32 v3, 31, v2
	v_ashrrev_i32_e32 v5, 31, v4
	v_lshl_add_u64 v[0:1], s[2:3], 1, v[32:33]
	v_lshlrev_b64 v[2:3], 10, v[2:3]
	v_lshlrev_b64 v[4:5], 10, v[4:5]
	v_lshl_add_u64 v[2:3], v[0:1], 0, v[2:3]
	v_lshl_add_u64 v[4:5], v[0:1], 0, v[4:5]
	global_load_dwordx4 v[60:63], v[2:3], off
	global_load_dwordx4 v[64:67], v[4:5], off
	v_add_u32_e32 v2, s11, v43
	v_add_u32_e32 v4, s11, v44
	v_ashrrev_i32_e32 v3, 31, v2
	v_ashrrev_i32_e32 v5, 31, v4
	v_lshlrev_b64 v[2:3], 10, v[2:3]
	v_lshlrev_b64 v[4:5], 10, v[4:5]
	v_lshl_add_u64 v[2:3], v[0:1], 0, v[2:3]
	v_lshl_add_u64 v[4:5], v[0:1], 0, v[4:5]
	global_load_dwordx4 v[68:71], v[2:3], off
	global_load_dwordx4 v[72:75], v[4:5], off
	v_add_u32_e32 v2, s11, v45
	v_add_u32_e32 v4, s11, v46
	v_ashrrev_i32_e32 v3, 31, v2
	v_ashrrev_i32_e32 v5, 31, v4
	v_lshlrev_b64 v[2:3], 10, v[2:3]
	v_lshlrev_b64 v[4:5], 10, v[4:5]
	v_lshl_add_u64 v[2:3], v[0:1], 0, v[2:3]
	v_lshl_add_u64 v[4:5], v[0:1], 0, v[4:5]
	global_load_dwordx4 v[76:79], v[2:3], off
	global_load_dwordx4 v[80:83], v[4:5], off
	v_add_u32_e32 v2, s11, v47
	v_add_u32_e32 v4, s11, v48
	v_ashrrev_i32_e32 v3, 31, v2
	v_ashrrev_i32_e32 v5, 31, v4
	v_lshlrev_b64 v[2:3], 10, v[2:3]
	v_lshlrev_b64 v[4:5], 10, v[4:5]
	v_lshl_add_u64 v[2:3], v[0:1], 0, v[2:3]
	v_lshl_add_u64 v[0:1], v[0:1], 0, v[4:5]
	s_lshl_b32 s0, s0, 8
	global_load_dwordx4 v[84:87], v[2:3], off
	global_load_dwordx4 v[88:91], v[0:1], off
	v_add_u32_e32 v0, s0, v38
	v_ashrrev_i32_e32 v1, 31, v0
	v_lshlrev_b64 v[0:1], 8, v[0:1]
	v_lshl_add_u64 v[58:59], v[34:35], 0, v[0:1]
	v_add_u32_e32 v0, s0, v39
	v_ashrrev_i32_e32 v1, 31, v0
	v_lshlrev_b64 v[0:1], 8, v[0:1]
	v_lshl_add_u64 v[92:93], v[34:35], 0, v[0:1]
	global_load_dwordx4 v[0:3], v[58:59], off
	global_load_dwordx4 v[4:7], v[58:59], off offset:64
	global_load_dwordx4 v[8:11], v[92:93], off
	global_load_dwordx4 v[12:15], v[92:93], off offset:64
	global_load_dwordx4 v[16:19], v[58:59], off offset:128
	global_load_dwordx4 v[20:23], v[58:59], off offset:192
	global_load_dwordx4 v[24:27], v[92:93], off offset:128
	global_load_dwordx4 v[28:31], v[92:93], off offset:192
	s_lshl_b32 s0, s9, 6
	s_mov_b32 s3, s1
	v_mov_b32_e32 v58, v49
	s_or_b32 s9, s0, s10
	v_add_u32_e32 v59, s2, v40
	s_mov_b32 s2, s1
	s_waitcnt vmcnt(16)
	s_barrier
	s_cmp_lg_u32 s99, 0
	s_cbranch_scc1 .Lsc1_post_skip
	v_readlane_b32 s99, v235, 9
	v_readlane_b32 s100, v235, 7
	v_readlane_b32 s101, v235, 8
	s_lshl_b32 s99, s99, 8
	s_addk_i32 s99, 0x1c00
	v_mov_b32_e32 v236, s99
	v_mov_b32_e32 v237, 1
	s_mov_b64 exec, 1
	s_nop 1
	global_atomic_add v238, v236, v237, s[100:101] sc0
	s_mov_b64 exec, -1
	s_mov_b32 s99, 1
.Lsc1_post_skip:
	s_waitcnt vmcnt(15)
	ds_write_b128 v50, v[60:63]
	s_waitcnt vmcnt(14)
	ds_write_b128 v51, v[64:67]
	s_waitcnt vmcnt(13)
	ds_write_b128 v52, v[68:71]
	s_waitcnt vmcnt(12)
	ds_write_b128 v53, v[72:75]
	s_waitcnt vmcnt(11)
	ds_write_b128 v54, v[76:79]
	s_waitcnt vmcnt(10)
	ds_write_b128 v55, v[80:83]
	s_waitcnt vmcnt(9)
	ds_write_b128 v56, v[84:87]
	s_waitcnt vmcnt(8)
	ds_write_b128 v57, v[88:91]
	s_waitcnt lgkmcnt(0)
	s_barrier
	s_waitcnt vmcnt(0)
	s_cmp_lg_u32 s99, 1
	s_cbranch_scc1 .Lsc1_chk_skip
	s_mov_b32 s99, 2
	v_mov_b32_e32 v239, 0x20000
	ds_read_b32 v239, v239
	v_add_u32_e32 v238, 1, v238
	s_waitcnt lgkmcnt(0)
	v_readfirstlane_b32 s100, v238
	v_readfirstlane_b32 s101, v239
	s_nop 0
	s_cmp_lg_u32 s100, s101
	s_cbranch_scc1 .Lsc1_chk_skip
	buffer_wbl2 sc1
	s_waitcnt vmcnt(0)
	v_readlane_b32 s100, v235, 7
	v_readlane_b32 s101, v235, 8
	v_mov_b32_e32 v236, 0x2c00
	v_mov_b32_e32 v237, 1
	s_mov_b64 exec, 1
	s_nop 3
	global_atomic_add v236, v237, s[100:101]
	s_mov_b64 exec, -1

.LBB0_494:
	v_writelane_b32 v235, s20, 19
	s_or_b64 exec, exec, s[2:3]
	v_readfirstlane_b32 s99, v186
	s_nop 0
	s_cmp_lg_u32 s99, 0
	s_cselect_b32 s99, 2, 0
	v_mov_b32_e32 v0, v186
	s_and_b64 vcc, exec, s[6:7]
	s_cbranch_vccnz .LBB0_499
	v_and_b32_e32 v3, 63, v0
	s_load_dwordx2 s[14:15], s[14:15], 0x50
	v_mov_b32_e32 v123, 0
	v_lshlrev_b32_e32 v122, 1, v3
	v_lshlrev_b32_e32 v2, 4, v0
	s_waitcnt lgkmcnt(0)
	v_lshl_add_u64 v[6:7], s[0:1], 0, v[122:123]
	s_mov_b64 s[16:17], 0x166f3000
	v_and_b32_e32 v1, 15, v0
	v_and_b32_e32 v120, 0x70, v2
	v_lshl_add_u64 v[124:125], v[6:7], 0, s[16:17]
	v_mbcnt_hi_u32_b32 v7, -1, v187
	v_ashrrev_i32_e32 v121, 6, v0
	v_ashrrev_i32_e32 v135, 3, v0
	v_ashrrev_i32_e32 v152, 4, v0
	v_lshlrev_b32_e32 v2, 2, v120
	v_lshl_add_u32 v8, v1, 2, 0
	v_bfe_u32 v9, v0, 4, 2
	v_mov_b32_e32 v3, v123
	v_and_b32_e32 v0, 0xffffffc0, v0
	v_and_b32_e32 v10, 64, v7
	v_add_u32_e32 v5, 0, v2
	v_lshl_add_u64 v[126:127], s[14:15], 0, v[2:3]
	v_mad_u32_u24 v2, v1, 12, v8
	v_add_u32_e32 v0, v8, v0
	v_xor_b32_e32 v8, 1, v7
	v_add_u32_e32 v10, 64, v10
	v_cmp_lt_i32_e32 vcc, v8, v10
	s_add_u32 s2, s0, 0xf1f3000
	s_addc_u32 s3, s1, 0
	v_cndmask_b32_e32 v8, v7, v8, vcc
	v_lshlrev_b32_e32 v153, 2, v8
	v_xor_b32_e32 v8, 2, v7
	v_cmp_lt_i32_e32 vcc, v8, v10
	s_add_u32 s6, s0, 0xe173000
	s_addc_u32 s7, s1, 0
	v_cndmask_b32_e32 v8, v7, v8, vcc
	v_lshlrev_b32_e32 v154, 2, v8
	v_xor_b32_e32 v8, 4, v7
	s_add_u32 s8, s0, 0x1771b000
	s_movk_i32 s12, 0x210
	v_cmp_lt_i32_e32 vcc, v8, v10
	s_addc_u32 s9, s1, 0
	v_lshlrev_b32_e32 v3, 3, v9
	v_mul_lo_u32 v6, v135, s12
	v_cndmask_b32_e32 v7, v7, v8, vcc
	s_movk_i32 s12, 0x110
	v_mul_u32_u24_e32 v8, 0x110, v1
	v_readlane_b32 s20, v235, 0
	s_add_u32 s10, s0, 0x1871b000
	v_lshlrev_b32_e32 v4, 3, v1
	v_lshlrev_b32_e32 v155, 2, v7
	v_mul_lo_u32 v7, v152, s12
	v_add3_u32 v156, 0, v3, v8
	v_mul_u32_u24_e32 v3, 0x840, v9
	v_lshlrev_b32_e32 v122, 4, v1
	v_readlane_b32 s26, v235, 16
	v_readlane_b32 s21, v235, 1
	v_readlane_b32 s22, v235, 2
	v_readlane_b32 s23, v235, 3
	s_addc_u32 s11, s1, 0
	s_mov_b32 s13, 0
	v_add_u32_e32 v157, 0x400, v121
	v_lshl_add_u64 v[128:129], s[2:3], 0, v[122:123]
	s_lshl_b32 s18, s26, 8
	s_lshl_b32 s19, s22, 8
	v_lshlrev_b32_e32 v130, 1, v4
	v_mov_b32_e32 v131, v123
	s_mov_b64 s[14:15], 0x10000
	s_mov_b32 s20, 0x10000
	v_mov_b32_e32 v158, 0x358637bd
	s_mov_b32 s21, 0x800000
	s_mov_b64 s[16:17], 0x1971b400
	s_mov_b32 s22, 0x1971b000
	v_add_u32_e32 v159, v2, v7
	v_add_u32_e32 v160, v0, v3
	v_add_u32_e32 v161, v5, v6
	s_mov_b32 s23, s26
	v_readlane_b32 s27, v235, 17

.LBB0_497:
	v_add_u32_e32 v18, s26, v162
	v_add_u32_e32 v16, 64, v18
	v_add_u32_e32 v18, 0x60, v18
	v_ashrrev_i32_e32 v17, 31, v16
	v_ashrrev_i32_e32 v19, 31, v18
	v_lshlrev_b64 v[16:17], 11, v[16:17]
	v_lshlrev_b64 v[18:19], 11, v[18:19]
	v_lshl_add_u64 v[16:17], v[136:137], 0, v[16:17]
	v_lshl_add_u64 v[18:19], v[136:137], 0, v[18:19]
	v_add_u32_e32 v138, s26, v133
	ds_write_b128 v159, v[52:55]
	ds_write_b128 v159, v[64:67] offset:8704
	ds_write_b128 v159, v[56:59] offset:17408
	ds_write_b128 v159, v[60:63] offset:26112
	s_waitcnt lgkmcnt(0)
	s_barrier
	s_cmp_lg_u32 s99, 0
	s_cbranch_scc1 .Lsc2_post_skip
	v_readlane_b32 s99, v235, 9
	v_readlane_b32 s100, v235, 7
	v_readlane_b32 s101, v235, 8
	s_lshl_b32 s99, s99, 8
	s_addk_i32 s99, 0x1c80
	v_mov_b32_e32 v236, s99
	v_mov_b32_e32 v237, 1
	s_mov_b64 exec, 1
	s_nop 1
	global_atomic_add v238, v236, v237, s[100:101] sc0
	s_mov_b64 exec, -1
	s_mov_b32 s99, 1
.Lsc2_post_skip:
	global_load_dwordx4 v[52:55], v[16:17], off nt
	global_load_dwordx4 v[64:67], v[18:19], off nt
	global_load_dwordx4 v[56:59], v[16:17], off offset:1024 nt
	global_load_dwordx4 v[60:63], v[18:19], off offset:1024 nt
	v_add_u32_e32 v16, 64, v138
	v_ashrrev_i32_e32 v17, 31, v16
	v_lshlrev_b64 v[16:17], 10, v[16:17]
	v_lshl_or_b32 v16, v134, 1, v16
	v_lshl_add_u64 v[18:19], s[8:9], 0, v[16:17]
	global_load_dwordx4 v[40:43], v[18:19], off offset:16 nt
	global_load_dwordx4 v[24:27], v[18:19], off nt
	v_lshl_add_u64 v[18:19], s[10:11], 0, v[16:17]
	v_lshl_add_u64 v[16:17], s[6:7], 0, v[16:17]
	global_load_dwordx4 v[32:35], v[18:19], off offset:16 nt
	global_load_dwordx4 v[20:23], v[18:19], off nt
	global_load_dwordx4 v[36:39], v[16:17], off offset:16 nt
	s_nop 0
	global_load_dwordx4 v[16:19], v[16:17], off nt
	ds_read2_b64 v[112:115], v156 offset1:4
	ds_read2_b64 v[148:151], v156 offset0:8 offset1:12
	v_add_u32_e32 v163, 0x1000, v156
	s_waitcnt lgkmcnt(1)
	v_mfma_f32_16x16x32_bf16 v[112:115], v[112:115], v[84:87], 0
	ds_read2_b64 v[116:119], v163 offset0:32 offset1:36
	v_add_u32_e32 v164, 0x2000, v156
	ds_read2_b64 v[140:143], v164 offset0:64 offset1:68
	s_waitcnt lgkmcnt(2)
	v_mfma_f32_16x16x32_bf16 v[112:115], v[148:151], v[80:83], v[112:115]
	ds_read2_b64 v[148:151], v163 offset0:40 offset1:44
	v_add_u32_e32 v165, 0x3000, v156
	ds_read2_b64 v[144:147], v165 offset0:96 offset1:100
	s_waitcnt lgkmcnt(3)
	v_mfma_f32_16x16x32_bf16 v[116:119], v[116:119], v[84:87], 0
	v_add_u32_e32 v166, 0x4000, v156
	v_add_u32_e32 v167, 0x5000, v156
	v_add_u32_e32 v168, 0x6000, v156
	s_waitcnt lgkmcnt(1)
	v_mfma_f32_16x16x32_bf16 v[116:119], v[148:151], v[80:83], v[116:119]
	ds_read2_b64 v[148:151], v164 offset0:72 offset1:76
	v_add_u32_e32 v169, 0x7000, v156
	v_add_u32_e32 v170, 0x8800, v160
	v_mfma_f32_16x16x32_bf16 v[140:143], v[140:143], v[84:87], 0
	v_add_u32_e32 v171, 0x8c00, v160
	v_add_u32_e32 v172, 0xa800, v160
	v_add_u32_e32 v173, 0xac00, v160
	s_waitcnt lgkmcnt(0)
	v_mfma_f32_16x16x32_bf16 v[140:143], v[148:151], v[80:83], v[140:143]
	ds_read2_b64 v[148:151], v165 offset0:104 offset1:108
	v_add_u32_e32 v174, 0xca00, v160
	v_add_u32_e32 v175, 0xce00, v160
	v_mfma_f32_16x16x32_bf16 v[144:147], v[144:147], v[84:87], 0
	v_add_u32_e32 v176, 0xea00, v160
	v_add_u32_e32 v177, 0xee00, v160
	v_ashrrev_i32_e32 v139, 31, v138
	s_waitcnt lgkmcnt(0)
	v_mfma_f32_16x16x32_bf16 v[144:147], v[148:151], v[80:83], v[144:147]
	ds_read2_b64 v[148:151], v156 offset0:16 offset1:20
	v_lshlrev_b32_e32 v122, 1, v120
	s_add_i32 s26, s26, 64
	s_waitcnt lgkmcnt(0)
	v_mfma_f32_16x16x32_bf16 v[112:115], v[148:151], v[76:79], v[112:115]
	ds_read2_b64 v[148:151], v163 offset0:48 offset1:52
	s_cmpk_eq_i32 s26, 0xc0
	s_waitcnt lgkmcnt(0)
	v_mfma_f32_16x16x32_bf16 v[116:119], v[148:151], v[76:79], v[116:119]
	ds_read2_b64 v[148:151], v164 offset0:80 offset1:84
	s_waitcnt lgkmcnt(0)
	v_mfma_f32_16x16x32_bf16 v[140:143], v[148:151], v[76:79], v[140:143]
	ds_read2_b64 v[148:151], v165 offset0:112 offset1:116
	s_waitcnt lgkmcnt(0)
	v_mfma_f32_16x16x32_bf16 v[144:147], v[148:151], v[76:79], v[144:147]
	ds_read2_b64 v[148:151], v156 offset0:24 offset1:28
	s_waitcnt lgkmcnt(0)
	v_mfma_f32_16x16x32_bf16 v[112:115], v[148:151], v[72:75], v[112:115]
	ds_read2_b64 v[148:151], v163 offset0:56 offset1:60
	s_waitcnt lgkmcnt(0)
	v_mfma_f32_16x16x32_bf16 v[116:119], v[148:151], v[72:75], v[116:119]
	ds_read2_b64 v[148:151], v164 offset0:88 offset1:92
	s_waitcnt lgkmcnt(0)
	v_mfma_f32_16x16x32_bf16 v[140:143], v[148:151], v[72:75], v[140:143]
	ds_read2_b64 v[148:151], v165 offset0:120 offset1:124
	s_waitcnt lgkmcnt(0)
	v_mfma_f32_16x16x32_bf16 v[144:147], v[148:151], v[72:75], v[144:147]
	ds_read2_b64 v[148:151], v166 offset0:128 offset1:132
	s_waitcnt lgkmcnt(0)
	v_mfma_f32_16x16x32_bf16 v[112:115], v[148:151], v[68:71], v[112:115]
	ds_read2_b64 v[148:151], v167 offset0:160 offset1:164
	s_waitcnt lgkmcnt(0)
	v_mfma_f32_16x16x32_bf16 v[116:119], v[148:151], v[68:71], v[116:119]
	ds_read2_b64 v[148:151], v168 offset0:192 offset1:196
	s_waitcnt lgkmcnt(0)
	v_mfma_f32_16x16x32_bf16 v[140:143], v[148:151], v[68:71], v[140:143]
	ds_read2_b64 v[148:151], v169 offset0:224 offset1:228
	s_waitcnt lgkmcnt(0)
	v_mfma_f32_16x16x32_bf16 v[144:147], v[148:151], v[68:71], v[144:147]
	ds_read2_b64 v[148:151], v166 offset0:136 offset1:140
	s_waitcnt lgkmcnt(0)
	v_mfma_f32_16x16x32_bf16 v[112:115], v[148:151], v[48:51], v[112:115]
	ds_read2_b64 v[148:151], v167 offset0:168 offset1:172
	s_waitcnt lgkmcnt(0)
	v_mfma_f32_16x16x32_bf16 v[116:119], v[148:151], v[48:51], v[116:119]
	ds_read2_b64 v[148:151], v168 offset0:200 offset1:204
	s_waitcnt lgkmcnt(0)
	v_mfma_f32_16x16x32_bf16 v[140:143], v[148:151], v[48:51], v[140:143]
	ds_read2_b64 v[148:151], v169 offset0:232 offset1:236
	s_waitcnt lgkmcnt(0)
	v_mfma_f32_16x16x32_bf16 v[144:147], v[148:151], v[48:51], v[144:147]
	ds_read2_b64 v[148:151], v166 offset0:144 offset1:148
	s_waitcnt lgkmcnt(0)
	v_mfma_f32_16x16x32_bf16 v[112:115], v[148:151], v[44:47], v[112:115]
	ds_read2_b64 v[148:151], v167 offset0:176 offset1:180
	s_waitcnt lgkmcnt(0)
	v_mfma_f32_16x16x32_bf16 v[116:119], v[148:151], v[44:47], v[116:119]
	ds_read2_b64 v[148:151], v168 offset0:208 offset1:212
	s_waitcnt lgkmcnt(0)
	v_mfma_f32_16x16x32_bf16 v[140:143], v[148:151], v[44:47], v[140:143]
	ds_read2_b64 v[148:151], v169 offset0:240 offset1:244
	s_waitcnt lgkmcnt(0)
	v_mfma_f32_16x16x32_bf16 v[144:147], v[148:151], v[44:47], v[144:147]
	ds_read2_b64 v[148:151], v166 offset0:152 offset1:156
	s_waitcnt lgkmcnt(0)
	v_mfma_f32_16x16x32_bf16 v[112:115], v[148:151], v[28:31], v[112:115]
	ds_read2_b64 v[148:151], v167 offset0:184 offset1:188
	s_waitcnt lgkmcnt(0)
	v_mfma_f32_16x16x32_bf16 v[116:119], v[148:151], v[28:31], v[116:119]
	ds_read2_b64 v[148:151], v168 offset0:216 offset1:220
	s_waitcnt lgkmcnt(0)
	v_mfma_f32_16x16x32_bf16 v[140:143], v[148:151], v[28:31], v[140:143]
	ds_read2_b64 v[148:151], v169 offset0:248 offset1:252
	s_nop 0
	ds_write2_b32 v170, v112, v113 offset1:132
	ds_write2_b32 v171, v114, v115 offset0:8 offset1:140
	s_waitcnt lgkmcnt(2)
	v_mfma_f32_16x16x32_bf16 v[144:147], v[148:151], v[28:31], v[144:147]
	ds_write2_b32 v172, v116, v117 offset0:64 offset1:196
	ds_write2_b32 v173, v118, v119 offset0:72 offset1:204
	ds_write2_b32 v174, v140, v141 offset1:132
	ds_write2_b32 v175, v142, v143 offset0:8 offset1:140
	s_nop 3
	ds_write2_b32 v176, v144, v145 offset0:64 offset1:196
	ds_write2_b32 v177, v146, v147 offset0:72 offset1:204
	s_waitcnt lgkmcnt(0)
	s_barrier
	s_cmp_lg_u32 s99, 1
	s_cbranch_scc1 .Lsc2_chk_skip
	s_mov_b32 s99, 2
	s_waitcnt vmcnt(10)
	v_mov_b32_e32 v239, 0x20000
	ds_read_b32 v239, v239
	v_add_u32_e32 v238, 1, v238
	s_waitcnt lgkmcnt(0)
	v_readfirstlane_b32 s100, v238
	v_readfirstlane_b32 s101, v239
	s_nop 0
	s_cmp_lg_u32 s100, s101
	s_cbranch_scc1 .Lsc2_chk_skip
	buffer_wbl2 sc1
	s_waitcnt vmcnt(0)
	v_readlane_b32 s100, v235, 7
	v_readlane_b32 s101, v235, 8
	v_mov_b32_e32 v236, 0x2c80
	v_mov_b32_e32 v237, 1
	s_mov_b64 exec, 1
	s_nop 3
	global_atomic_add v236, v237, s[100:101]
	s_mov_b64 exec, -1
.Lsc2_chk_skip:
	s_cmpk_eq_i32 s26, 0xc0
	ds_read_b128 v[112:115], v161 offset:34816
	ds_read_b128 v[116:119], v161 offset:34832
	ds_read_b128 v[178:181], v161 offset:34848
	ds_read_b128 v[146:149], v161 offset:34864
	v_lshlrev_b32_e32 v140, 16, v103
	v_and_b32_e32 v141, 0xffff0000, v103
	v_lshlrev_b32_e32 v142, 16, v111
	v_and_b32_e32 v143, 0xffff0000, v111
	v_pk_add_f32 v[140:141], v[142:143], v[140:141]
	v_and_b32_e32 v103, 0xffff0000, v110
	s_waitcnt lgkmcnt(0)
	v_pk_add_f32 v[140:141], v[140:141], v[148:149]
	v_lshlrev_b32_e32 v148, 16, v102
	v_and_b32_e32 v149, 0xffff0000, v102
	v_lshlrev_b32_e32 v102, 16, v110
	v_pk_add_f32 v[102:103], v[102:103], v[148:149]
	v_lshlrev_b32_e32 v142, 16, v107
	v_pk_add_f32 v[102:103], v[102:103], v[146:147]
	v_lshlrev_b32_e32 v146, 16, v106
	v_and_b32_e32 v147, 0xffff0000, v106
	v_and_b32_e32 v143, 0xffff0000, v107
	v_mul_f32_e32 v106, 0xbfb8aa3b, v146
	v_mul_f32_e32 v107, 0xbfb8aa3b, v147
	v_exp_f32_e32 v106, v106
	v_exp_f32_e32 v107, v107
	v_lshlrev_b32_e32 v148, 16, v109
	v_and_b32_e32 v149, 0xffff0000, v109
	v_add_f32_e32 v106, 1.0, v106
	v_add_f32_e32 v107, 1.0, v107
	v_rcp_f32_e32 v106, v106
	v_rcp_f32_e32 v107, v107
	v_pk_mul_f32 v[110:111], v[102:103], v[102:103]
	v_pk_mul_f32 v[144:145], v[140:141], v[140:141]
	v_pk_mul_f32 v[106:107], v[106:107], v[146:147]
	v_lshlrev_b32_e32 v146, 16, v101
	v_and_b32_e32 v147, 0xffff0000, v101
	v_pk_add_f32 v[146:147], v[148:149], v[146:147]
	v_lshlrev_b32_e32 v148, 16, v105
	v_mul_f32_e32 v101, 0xbfb8aa3b, v148
	v_exp_f32_e32 v101, v101
	v_and_b32_e32 v149, 0xffff0000, v105
	v_pk_add_f32 v[146:147], v[146:147], v[180:181]
	v_add_f32_e32 v101, 1.0, v101
	v_rcp_f32_e32 v180, v101
	v_mul_f32_e32 v101, 0xbfb8aa3b, v149
	v_exp_f32_e32 v101, v101
	v_pk_mul_f32 v[150:151], v[146:147], v[146:147]
	v_add_f32_e32 v101, 1.0, v101
	v_rcp_f32_e32 v181, v101
	v_and_b32_e32 v101, 0xffff0000, v108
	v_pk_mul_f32 v[148:149], v[180:181], v[148:149]
	v_lshlrev_b32_e32 v180, 16, v100
	v_and_b32_e32 v181, 0xffff0000, v100
	v_lshlrev_b32_e32 v100, 16, v108
	v_pk_add_f32 v[100:101], v[100:101], v[180:181]
	v_lshlrev_b32_e32 v180, 16, v99
	v_pk_add_f32 v[100:101], v[100:101], v[178:179]
	v_lshlrev_b32_e32 v178, 16, v104
	v_and_b32_e32 v179, 0xffff0000, v104
	v_mul_f32_e32 v104, 0xbfb8aa3b, v178
	v_mul_f32_e32 v105, 0xbfb8aa3b, v179
	v_exp_f32_e32 v104, v104
	v_exp_f32_e32 v105, v105
	v_and_b32_e32 v181, 0xffff0000, v99
	v_and_b32_e32 v99, 0xffff0000, v94
	v_add_f32_e32 v104, 1.0, v104
	v_add_f32_e32 v105, 1.0, v105
	v_rcp_f32_e32 v104, v104
	v_rcp_f32_e32 v105, v105
	v_pk_mul_f32 v[108:109], v[100:101], v[100:101]
	v_pk_mul_f32 v[104:105], v[104:105], v[178:179]
	v_lshlrev_b32_e32 v178, 16, v91
	v_and_b32_e32 v179, 0xffff0000, v91
	v_pk_add_f32 v[178:179], v[180:181], v[178:179]
	s_nop 0
	v_pk_add_f32 v[118:119], v[178:179], v[118:119]
	v_lshlrev_b32_e32 v178, 16, v95
	v_mul_f32_e32 v91, 0xbfb8aa3b, v178
	v_exp_f32_e32 v91, v91
	v_and_b32_e32 v179, 0xffff0000, v95
	v_pk_mul_f32 v[180:181], v[118:119], v[118:119]
	v_add_f32_e32 v91, 1.0, v91
	v_rcp_f32_e32 v182, v91
	v_mul_f32_e32 v91, 0xbfb8aa3b, v179
	v_exp_f32_e32 v91, v91
	s_nop 0
	v_add_f32_e32 v91, 1.0, v91
	v_rcp_f32_e32 v183, v91
	v_and_b32_e32 v91, 0xffff0000, v98
	v_pk_mul_f32 v[178:179], v[182:183], v[178:179]
	v_lshlrev_b32_e32 v182, 16, v90
	v_and_b32_e32 v183, 0xffff0000, v90
	v_lshlrev_b32_e32 v90, 16, v98
	v_pk_add_f32 v[90:91], v[90:91], v[182:183]
	v_lshlrev_b32_e32 v98, 16, v94
	v_pk_add_f32 v[90:91], v[90:91], v[116:117]
	v_mul_f32_e32 v116, 0xbfb8aa3b, v98
	v_mul_f32_e32 v117, 0xbfb8aa3b, v99
	v_exp_f32_e32 v116, v116
	v_exp_f32_e32 v117, v117
	v_lshlrev_b32_e32 v182, 16, v97
	v_and_b32_e32 v183, 0xffff0000, v97
	v_add_f32_e32 v116, 1.0, v116
	v_add_f32_e32 v117, 1.0, v117
	v_rcp_f32_e32 v116, v116
	v_rcp_f32_e32 v117, v117
	v_and_b32_e32 v97, 0xffff0000, v92
	v_pk_mul_f32 v[94:95], v[90:91], v[90:91]
	v_pk_mul_f32 v[98:99], v[116:117], v[98:99]
	v_lshlrev_b32_e32 v116, 16, v89
	v_and_b32_e32 v117, 0xffff0000, v89
	v_pk_add_f32 v[116:117], v[182:183], v[116:117]
	s_nop 0
	v_pk_add_f32 v[114:115], v[116:117], v[114:115]
	v_lshlrev_b32_e32 v116, 16, v93
	v_mul_f32_e32 v89, 0xbfb8aa3b, v116
	v_exp_f32_e32 v89, v89
	v_and_b32_e32 v117, 0xffff0000, v93
	v_pk_mul_f32 v[182:183], v[114:115], v[114:115]
	v_add_f32_e32 v89, 1.0, v89
	v_rcp_f32_e32 v184, v89
	v_mul_f32_e32 v89, 0xbfb8aa3b, v117
	v_exp_f32_e32 v89, v89
	s_nop 0
	v_add_f32_e32 v89, 1.0, v89
	v_rcp_f32_e32 v185, v89
	v_and_b32_e32 v89, 0xffff0000, v96
	v_pk_mul_f32 v[116:117], v[184:185], v[116:117]
	v_lshlrev_b32_e32 v184, 16, v88
	v_and_b32_e32 v185, 0xffff0000, v88
	v_lshlrev_b32_e32 v88, 16, v96
	v_pk_add_f32 v[88:89], v[88:89], v[184:185]
	v_lshlrev_b32_e32 v96, 16, v92
	v_pk_add_f32 v[88:89], v[88:89], v[112:113]
	v_mul_f32_e32 v112, 0xbfb8aa3b, v96
	v_pk_mul_f32 v[92:93], v[88:89], v[88:89]
	v_mul_f32_e32 v113, 0xbfb8aa3b, v97
	v_add_f32_e32 v92, v92, v93
	v_add_f32_e32 v92, v182, v92
	v_add_f32_e32 v92, v183, v92
	v_add_f32_e32 v92, v94, v92
	v_add_f32_e32 v92, v95, v92
	v_add_f32_e32 v92, v180, v92
	v_add_f32_e32 v92, v181, v92
	v_add_f32_e32 v92, v108, v92
	v_add_f32_e32 v92, v109, v92
	v_add_f32_e32 v92, v150, v92
	v_add_f32_e32 v92, v151, v92
	v_add_f32_e32 v92, v110, v92
	v_add_f32_e32 v92, v111, v92
	v_add_f32_e32 v92, v144, v92
	v_add_f32_e32 v92, v145, v92
	ds_bpermute_b32 v93, v153, v92
	v_exp_f32_e32 v112, v112
	v_exp_f32_e32 v113, v113
	s_waitcnt vmcnt(3)
	v_mov_b64_e32 v[110:111], v[34:35]
	v_mov_b64_e32 v[108:109], v[32:33]
	s_waitcnt lgkmcnt(0)
	v_add_f32_e32 v92, v92, v93
	ds_bpermute_b32 v93, v154, v92
	v_add_f32_e32 v112, 1.0, v112
	v_add_f32_e32 v113, 1.0, v113
	v_rcp_f32_e32 v112, v112
	v_rcp_f32_e32 v113, v113
	s_waitcnt lgkmcnt(0)
	v_add_f32_e32 v92, v92, v93
	ds_bpermute_b32 v93, v155, v92
	v_pk_mul_f32 v[96:97], v[112:113], v[96:97]
	s_waitcnt lgkmcnt(0)
	v_add_f32_e32 v92, v92, v93
	v_fmamk_f32 v92, v92, 0x3c000000, v158
	v_cmp_gt_f32_e32 vcc, s21, v92
	v_mul_f32_e32 v93, 0x4b800000, v92
	s_nop 0
	v_cndmask_b32_e32 v92, v92, v93, vcc
	v_rsq_f32_e32 v92, v92
	s_nop 0
	v_mul_f32_e32 v93, 0x45800000, v92
	v_cndmask_b32_e32 v92, v92, v93, vcc
	v_pk_mul_f32 v[90:91], v[90:91], v[92:93] op_sel_hi:[1,0]
	v_pk_mul_f32 v[88:89], v[88:89], v[92:93] op_sel_hi:[1,0]
	v_pk_mul_f32 v[90:91], v[8:9], v[90:91]
	v_pk_mul_f32 v[88:89], v[12:13], v[88:89]
	v_pk_mul_f32 v[90:91], v[98:99], v[90:91]
	v_pk_mul_f32 v[98:99], v[100:101], v[92:93] op_sel_hi:[1,0]
	v_pk_mul_f32 v[88:89], v[96:97], v[88:89]
	v_pk_mul_f32 v[98:99], v[4:5], v[98:99]
	v_pk_mul_f32 v[94:95], v[114:115], v[92:93] op_sel_hi:[1,0]
	v_pk_mul_f32 v[96:97], v[118:119], v[92:93] op_sel_hi:[1,0]
	v_pk_mul_f32 v[98:99], v[104:105], v[98:99]
	v_pk_mul_f32 v[100:101], v[146:147], v[92:93] op_sel_hi:[1,0]
	v_pk_mul_f32 v[102:103], v[102:103], v[92:93] op_sel_hi:[1,0]
	v_mul_f32_e32 v93, 0xbfb8aa3b, v142
	v_mul_f32_e32 v105, 0xbfb8aa3b, v143
	v_exp_f32_e32 v93, v93
	v_exp_f32_e32 v105, v105
	v_pk_mul_f32 v[96:97], v[10:11], v[96:97]
	v_cvt_pk_bf16_f32 v90, v90, v91
	v_add_f32_e32 v93, 1.0, v93
	v_add_f32_e32 v105, 1.0, v105
	v_pk_mul_f32 v[96:97], v[178:179], v[96:97]
	v_rcp_f32_e32 v104, v93
	v_rcp_f32_e32 v105, v105
	v_cvt_pk_bf16_f32 v91, v96, v97
	v_lshlrev_b64 v[96:97], 11, v[138:139]
	v_lshl_add_u64 v[96:97], s[0:1], 0, v[96:97]
	v_pk_mul_f32 v[92:93], v[140:141], v[92:93] op_sel_hi:[1,0]
	v_lshl_add_u64 v[96:97], v[96:97], 0, s[12:13]
	v_pk_mul_f32 v[94:95], v[14:15], v[94:95]
	v_pk_mul_f32 v[100:101], v[6:7], v[100:101]
	v_pk_mul_f32 v[102:103], v[0:1], v[102:103]
	v_pk_mul_f32 v[92:93], v[2:3], v[92:93]
	v_pk_mul_f32 v[104:105], v[104:105], v[142:143]
	v_lshl_add_u64 v[96:97], v[96:97], 0, v[122:123]
	v_pk_mul_f32 v[94:95], v[116:117], v[94:95]
	v_pk_mul_f32 v[100:101], v[148:149], v[100:101]
	v_pk_mul_f32 v[102:103], v[106:107], v[102:103]
	v_pk_mul_f32 v[104:105], v[104:105], v[92:93]
	v_cvt_pk_bf16_f32 v92, v98, v99
	v_lshl_add_u64 v[98:99], v[96:97], 0, s[16:17]
	v_add_co_u32_e32 v96, vcc, 0x1971b000, v96
	v_cvt_pk_bf16_f32 v88, v88, v89
	v_cvt_pk_bf16_f32 v89, v94, v95
	v_cvt_pk_bf16_f32 v93, v100, v101
	v_cvt_pk_bf16_f32 v94, v102, v103
	v_cvt_pk_bf16_f32 v95, v104, v105
	v_addc_co_u32_e32 v97, vcc, 0, v97, vcc
	global_store_dwordx4 v[96:97], v[88:91], off offset:1024
	global_store_dwordx4 v[98:99], v[92:95], off offset:16
	s_waitcnt vmcnt(3)
	v_mov_b64_e32 v[106:107], v[38:39]
	v_mov_b64_e32 v[98:99], v[22:23]
	s_waitcnt vmcnt(2)
	v_mov_b64_e32 v[94:95], v[18:19]
	v_mov_b64_e32 v[102:103], v[42:43]
	v_mov_b64_e32 v[90:91], v[26:27]
	v_mov_b64_e32 v[104:105], v[36:37]
	v_mov_b64_e32 v[92:93], v[16:17]
	v_mov_b64_e32 v[96:97], v[20:21]
	v_mov_b64_e32 v[100:101], v[40:41]
	v_mov_b64_e32 v[88:89], v[24:25]
	s_cbranch_scc0 .LBB0_497
	ds_write_b128 v159, v[52:55]
	ds_write_b128 v159, v[64:67] offset:8704
	ds_write_b128 v159, v[56:59] offset:17408
	ds_write_b128 v159, v[60:63] offset:26112
	s_waitcnt lgkmcnt(0)
	s_barrier
	ds_read2_b64 v[52:55], v156 offset1:4
	ds_read2_b64 v[56:59], v163 offset0:32 offset1:36
	ds_read2_b64 v[60:63], v164 offset0:64 offset1:68
	ds_read2_b64 v[64:67], v165 offset0:96 offset1:100
	s_waitcnt lgkmcnt(3)
	v_mfma_f32_16x16x32_bf16 v[52:55], v[52:55], v[84:87], 0
	ds_read2_b64 v[88:91], v156 offset0:8 offset1:12
	v_readlane_b32 s28, v235, 0
	v_readlane_b32 s30, v235, 2
	s_waitcnt lgkmcnt(3)
	v_mfma_f32_16x16x32_bf16 v[56:59], v[56:59], v[84:87], 0
	s_add_i32 s23, s23, s30
	s_add_i32 s18, s18, s19
	s_cmpk_gt_i32 s23, 0xff
	s_waitcnt lgkmcnt(2)
	v_mfma_f32_16x16x32_bf16 v[60:63], v[60:63], v[84:87], 0
	v_readlane_b32 s29, v235, 1
	v_readlane_b32 s31, v235, 3
	s_waitcnt lgkmcnt(1)
	v_mfma_f32_16x16x32_bf16 v[64:67], v[64:67], v[84:87], 0
	ds_read2_b64 v[84:87], v163 offset0:40 offset1:44
	s_waitcnt lgkmcnt(1)
	v_mfma_f32_16x16x32_bf16 v[52:55], v[88:91], v[80:83], v[52:55]
	ds_read2_b64 v[88:91], v164 offset0:72 offset1:76
	s_waitcnt lgkmcnt(1)
	v_mfma_f32_16x16x32_bf16 v[56:59], v[84:87], v[80:83], v[56:59]
	ds_read2_b64 v[84:87], v165 offset0:104 offset1:108
	s_waitcnt lgkmcnt(1)
	v_mfma_f32_16x16x32_bf16 v[60:63], v[88:91], v[80:83], v[60:63]
	ds_read2_b64 v[88:91], v156 offset0:16 offset1:20
	s_waitcnt lgkmcnt(1)
	v_mfma_f32_16x16x32_bf16 v[64:67], v[84:87], v[80:83], v[64:67]
	ds_read2_b64 v[80:83], v163 offset0:48 offset1:52
	ds_read2_b64 v[84:87], v164 offset0:80 offset1:84
	s_waitcnt lgkmcnt(1)
	v_mfma_f32_16x16x32_bf16 v[56:59], v[80:83], v[76:79], v[56:59]
	ds_read2_b64 v[80:83], v165 offset0:112 offset1:116
	v_mfma_f32_16x16x32_bf16 v[52:55], v[88:91], v[76:79], v[52:55]
	s_waitcnt lgkmcnt(1)
	v_mfma_f32_16x16x32_bf16 v[60:63], v[84:87], v[76:79], v[60:63]
	ds_read2_b64 v[84:87], v156 offset0:24 offset1:28
	s_waitcnt lgkmcnt(1)
	v_mfma_f32_16x16x32_bf16 v[64:67], v[80:83], v[76:79], v[64:67]
	ds_read2_b64 v[76:79], v163 offset0:56 offset1:60
	ds_read2_b64 v[80:83], v164 offset0:88 offset1:92
	s_waitcnt lgkmcnt(1)
	v_mfma_f32_16x16x32_bf16 v[56:59], v[76:79], v[72:75], v[56:59]
	ds_read2_b64 v[76:79], v165 offset0:120 offset1:124
	v_mfma_f32_16x16x32_bf16 v[52:55], v[84:87], v[72:75], v[52:55]
	s_waitcnt lgkmcnt(1)
	v_mfma_f32_16x16x32_bf16 v[60:63], v[80:83], v[72:75], v[60:63]
	ds_read2_b64 v[80:83], v166 offset0:128 offset1:132
	s_waitcnt lgkmcnt(1)
	v_mfma_f32_16x16x32_bf16 v[64:67], v[76:79], v[72:75], v[64:67]
	ds_read2_b64 v[72:75], v167 offset0:160 offset1:164
	ds_read2_b64 v[76:79], v168 offset0:192 offset1:196
	s_waitcnt lgkmcnt(1)
	v_mfma_f32_16x16x32_bf16 v[56:59], v[72:75], v[68:71], v[56:59]
	ds_read2_b64 v[72:75], v169 offset0:224 offset1:228
	v_mfma_f32_16x16x32_bf16 v[52:55], v[80:83], v[68:71], v[52:55]
	s_waitcnt lgkmcnt(1)
	v_mfma_f32_16x16x32_bf16 v[60:63], v[76:79], v[68:71], v[60:63]
	ds_read2_b64 v[76:79], v166 offset0:136 offset1:140
	s_waitcnt lgkmcnt(1)
	v_mfma_f32_16x16x32_bf16 v[64:67], v[72:75], v[68:71], v[64:67]
	ds_read2_b64 v[68:71], v167 offset0:168 offset1:172
	ds_read2_b64 v[72:75], v168 offset0:200 offset1:204
	s_waitcnt lgkmcnt(1)
	v_mfma_f32_16x16x32_bf16 v[56:59], v[68:71], v[48:51], v[56:59]
	ds_read2_b64 v[68:71], v169 offset0:232 offset1:236
	v_mfma_f32_16x16x32_bf16 v[52:55], v[76:79], v[48:51], v[52:55]
	s_waitcnt lgkmcnt(1)
	v_mfma_f32_16x16x32_bf16 v[60:63], v[72:75], v[48:51], v[60:63]
	ds_read2_b64 v[72:75], v166 offset0:144 offset1:148
	s_waitcnt lgkmcnt(1)
	v_mfma_f32_16x16x32_bf16 v[48:51], v[68:71], v[48:51], v[64:67]
	ds_read2_b64 v[68:71], v168 offset0:208 offset1:212
	s_nop 1
	ds_read2_b64 v[64:67], v167 offset0:176 offset1:180
	s_waitcnt lgkmcnt(0)
	v_mfma_f32_16x16x32_bf16 v[56:59], v[64:67], v[44:47], v[56:59]
	ds_read2_b64 v[64:67], v169 offset0:240 offset1:244
	v_mfma_f32_16x16x32_bf16 v[60:63], v[68:71], v[44:47], v[60:63]
	ds_read2_b64 v[68:71], v166 offset0:152 offset1:156
	v_mfma_f32_16x16x32_bf16 v[52:55], v[72:75], v[44:47], v[52:55]
	s_waitcnt lgkmcnt(1)
	v_mfma_f32_16x16x32_bf16 v[44:47], v[64:67], v[44:47], v[48:51]
	s_nop 2
	ds_read2_b64 v[48:51], v167 offset0:184 offset1:188
	s_waitcnt lgkmcnt(1)
	v_mfma_f32_16x16x32_bf16 v[52:55], v[68:71], v[28:31], v[52:55]
	ds_read2_b64 v[64:67], v168 offset0:216 offset1:220
	ds_read2_b64 v[68:71], v169 offset0:248 offset1:252
	s_waitcnt lgkmcnt(2)
	v_mfma_f32_16x16x32_bf16 v[48:51], v[48:51], v[28:31], v[56:59]
	s_nop 3
	ds_write2_b32 v170, v52, v53 offset1:132
	ds_write2_b32 v171, v54, v55 offset0:8 offset1:140
	s_nop 1
	ds_write2_b32 v172, v48, v49 offset0:64 offset1:196
	s_waitcnt lgkmcnt(4)
	v_mfma_f32_16x16x32_bf16 v[52:55], v[64:67], v[28:31], v[60:63]
	ds_write2_b32 v173, v50, v51 offset0:72 offset1:204
	s_nop 6
	ds_write2_b32 v174, v52, v53 offset1:132
	ds_write2_b32 v175, v54, v55 offset0:8 offset1:140
	s_waitcnt lgkmcnt(6)
	v_mfma_f32_16x16x32_bf16 v[28:31], v[68:71], v[28:31], v[44:47]
	v_lshlrev_b32_e32 v62, 16, v38
	v_and_b32_e32 v63, 0xffff0000, v38
	s_nop 5
	ds_write2_b32 v176, v28, v29 offset0:64 offset1:196
	ds_write2_b32 v177, v30, v31 offset0:72 offset1:204
	v_lshlrev_b32_e32 v30, 16, v35
	v_and_b32_e32 v31, 0xffff0000, v35
	v_mul_f32_e32 v35, 0xbfb8aa3b, v62
	v_mul_f32_e32 v38, 0xbfb8aa3b, v63
	v_exp_f32_e32 v35, v35
	v_exp_f32_e32 v38, v38
	v_lshlrev_b32_e32 v28, 16, v43
	v_and_b32_e32 v29, 0xffff0000, v43
	v_lshlrev_b32_e32 v60, 16, v42
	v_and_b32_e32 v61, 0xffff0000, v42
	v_lshlrev_b32_e32 v42, 16, v34
	v_and_b32_e32 v43, 0xffff0000, v34
	v_add_f32_e32 v34, 1.0, v35
	v_add_f32_e32 v35, 1.0, v38
	s_waitcnt lgkmcnt(0)
	s_barrier
	ds_read_b128 v[44:47], v161 offset:34816
	ds_read_b128 v[48:51], v161 offset:34832
	ds_read_b128 v[52:55], v161 offset:34848
	ds_read_b128 v[56:59], v161 offset:34864
	v_rcp_f32_e32 v34, v34
	v_rcp_f32_e32 v35, v35
	v_pk_add_f32 v[28:29], v[28:29], v[30:31]
	v_lshlrev_b32_e32 v70, 16, v24
	s_waitcnt lgkmcnt(0)
	v_pk_add_f32 v[30:31], v[28:29], v[58:59]
	v_pk_mul_f32 v[34:35], v[34:35], v[62:63]
	v_lshlrev_b32_e32 v62, 16, v37
	v_lshlrev_b32_e32 v28, 16, v39
	v_and_b32_e32 v29, 0xffff0000, v39
	v_pk_add_f32 v[38:39], v[60:61], v[42:43]
	v_and_b32_e32 v63, 0xffff0000, v37
	v_mul_f32_e32 v37, 0xbfb8aa3b, v62
	v_pk_add_f32 v[38:39], v[38:39], v[56:57]
	v_lshlrev_b32_e32 v56, 16, v41
	v_and_b32_e32 v57, 0xffff0000, v41
	v_exp_f32_e32 v37, v37
	v_mul_f32_e32 v41, 0xbfb8aa3b, v63
	v_exp_f32_e32 v41, v41
	v_lshlrev_b32_e32 v60, 16, v33
	v_and_b32_e32 v61, 0xffff0000, v33
	v_add_f32_e32 v33, 1.0, v37
	v_rcp_f32_e32 v64, v33
	v_add_f32_e32 v33, 1.0, v41
	v_rcp_f32_e32 v65, v33
	v_pk_add_f32 v[56:57], v[56:57], v[60:61]
	v_and_b32_e32 v41, 0xffff0000, v32
	v_and_b32_e32 v71, 0xffff0000, v24
	v_pk_mul_f32 v[60:61], v[64:65], v[62:63]
	v_lshlrev_b32_e32 v64, 16, v36
	v_and_b32_e32 v65, 0xffff0000, v36
	v_mul_f32_e32 v33, 0xbfb8aa3b, v64
	v_mul_f32_e32 v36, 0xbfb8aa3b, v65
	v_exp_f32_e32 v33, v33
	v_exp_f32_e32 v36, v36
	v_lshlrev_b32_e32 v62, 16, v40
	v_and_b32_e32 v63, 0xffff0000, v40
	v_lshlrev_b32_e32 v40, 16, v32
	v_add_f32_e32 v32, 1.0, v33
	v_add_f32_e32 v33, 1.0, v36
	v_rcp_f32_e32 v32, v32
	v_rcp_f32_e32 v33, v33
	v_pk_add_f32 v[36:37], v[62:63], v[40:41]
	v_lshlrev_b32_e32 v62, 16, v23
	v_pk_add_f32 v[36:37], v[36:37], v[52:53]
	v_pk_mul_f32 v[32:33], v[32:33], v[64:65]
	v_lshlrev_b32_e32 v64, 16, v19
	v_and_b32_e32 v65, 0xffff0000, v19
	v_mul_f32_e32 v19, 0xbfb8aa3b, v64
	v_lshlrev_b32_e32 v52, 16, v27
	v_and_b32_e32 v53, 0xffff0000, v27
	v_exp_f32_e32 v19, v19
	v_mul_f32_e32 v27, 0xbfb8aa3b, v65
	v_exp_f32_e32 v27, v27
	v_and_b32_e32 v63, 0xffff0000, v23
	v_add_f32_e32 v19, 1.0, v19
	v_rcp_f32_e32 v66, v19
	v_add_f32_e32 v19, 1.0, v27
	v_rcp_f32_e32 v67, v19
	v_pk_add_f32 v[52:53], v[52:53], v[62:63]
	v_and_b32_e32 v27, 0xffff0000, v22
	v_lshlrev_b32_e32 v24, 16, v20
	v_pk_mul_f32 v[62:63], v[66:67], v[64:65]
	v_lshlrev_b32_e32 v64, 16, v26
	v_and_b32_e32 v65, 0xffff0000, v26
	v_lshlrev_b32_e32 v26, 16, v22
	v_pk_add_f32 v[22:23], v[64:65], v[26:27]
	v_lshlrev_b32_e32 v64, 16, v25
	v_and_b32_e32 v65, 0xffff0000, v25
	v_lshlrev_b32_e32 v66, 16, v21
	v_and_b32_e32 v67, 0xffff0000, v21
	v_pk_add_f32 v[64:65], v[64:65], v[66:67]
	v_lshlrev_b32_e32 v66, 16, v17
	v_mul_f32_e32 v21, 0xbfb8aa3b, v66
	v_exp_f32_e32 v21, v21
	v_and_b32_e32 v25, 0xffff0000, v20
	v_and_b32_e32 v67, 0xffff0000, v17
	v_lshlrev_b32_e32 v26, 16, v18
	v_add_f32_e32 v17, 1.0, v21
	v_pk_add_f32 v[20:21], v[70:71], v[24:25]
	v_pk_add_f32 v[46:47], v[64:65], v[46:47]
	v_pk_add_f32 v[20:21], v[20:21], v[44:45]
	v_and_b32_e32 v27, 0xffff0000, v18
	v_pk_mul_f32 v[24:25], v[20:21], v[20:21]
	v_mul_f32_e32 v18, 0xbfb8aa3b, v26
	v_pk_mul_f32 v[64:65], v[46:47], v[46:47]
	v_add_f32_e32 v24, v24, v25
	v_pk_add_f32 v[22:23], v[22:23], v[48:49]
	v_exp_f32_e32 v48, v18
	v_mul_f32_e32 v18, 0xbfb8aa3b, v27
	v_add_f32_e32 v24, v64, v24
	v_exp_f32_e32 v49, v18
	v_pk_mul_f32 v[18:19], v[22:23], v[22:23]
	v_add_f32_e32 v24, v65, v24
	v_pk_add_f32 v[50:51], v[52:53], v[50:51]
	v_add_f32_e32 v18, v18, v24
	v_pk_mul_f32 v[52:53], v[50:51], v[50:51]
	v_add_f32_e32 v18, v19, v18
	v_add_f32_e32 v18, v52, v18
	v_pk_mul_f32 v[40:41], v[36:37], v[36:37]
	v_add_f32_e32 v18, v53, v18
	v_pk_add_f32 v[54:55], v[56:57], v[54:55]
	v_add_f32_e32 v18, v40, v18
	v_pk_mul_f32 v[56:57], v[54:55], v[54:55]
	v_add_f32_e32 v18, v41, v18
	v_add_f32_e32 v18, v56, v18
	v_pk_mul_f32 v[42:43], v[38:39], v[38:39]
	v_add_f32_e32 v18, v57, v18
	v_add_f32_e32 v18, v42, v18
	v_pk_mul_f32 v[58:59], v[30:31], v[30:31]
	v_add_f32_e32 v18, v43, v18
	v_add_f32_e32 v18, v58, v18
	v_add_f32_e32 v24, v59, v18
	v_rcp_f32_e32 v68, v17
	v_mul_f32_e32 v17, 0xbfb8aa3b, v67
	ds_bpermute_b32 v25, v153, v24
	v_exp_f32_e32 v17, v17
	v_lshlrev_b32_e32 v18, 16, v16
	v_and_b32_e32 v19, 0xffff0000, v16
	v_add_f32_e32 v48, 1.0, v48
	v_add_f32_e32 v17, 1.0, v17
	s_waitcnt lgkmcnt(0)
	v_add_f32_e32 v16, v24, v25
	v_rcp_f32_e32 v69, v17
	ds_bpermute_b32 v17, v154, v16
	v_mul_f32_e32 v24, 0xbfb8aa3b, v18
	v_exp_f32_e32 v24, v24
	v_mul_f32_e32 v25, 0xbfb8aa3b, v19
	v_exp_f32_e32 v25, v25
	s_waitcnt lgkmcnt(0)
	v_add_f32_e32 v40, v16, v17
	ds_bpermute_b32 v41, v155, v40
	v_add_f32_e32 v16, 1.0, v24
	v_add_f32_e32 v17, 1.0, v25
	v_rcp_f32_e32 v16, v16
	v_rcp_f32_e32 v17, v17
	s_waitcnt lgkmcnt(0)
	v_add_f32_e32 v24, v40, v41
	v_fmamk_f32 v24, v24, 0x3c000000, v158
	v_mul_f32_e32 v25, 0x4b800000, v24
	v_cmp_gt_f32_e32 vcc, s21, v24
	v_pk_mul_f32 v[16:17], v[16:17], v[18:19]
	v_add_f32_e32 v49, 1.0, v49
	v_cndmask_b32_e32 v24, v24, v25, vcc
	v_rsq_f32_e32 v40, v24
	v_rcp_f32_e32 v48, v48
	v_rcp_f32_e32 v49, v49
	v_mul_f32_e32 v18, 0x45800000, v40
	v_cndmask_b32_e32 v18, v40, v18, vcc
	v_pk_mul_f32 v[20:21], v[20:21], v[18:19] op_sel_hi:[1,0]
	v_pk_mul_f32 v[24:25], v[48:49], v[26:27]
	v_pk_mul_f32 v[12:13], v[12:13], v[20:21]
	v_mul_f32_e32 v20, 0xbfb8aa3b, v29
	v_pk_mul_f32 v[12:13], v[16:17], v[12:13]
	v_pk_mul_f32 v[16:17], v[46:47], v[18:19] op_sel_hi:[1,0]
	v_exp_f32_e32 v20, v20
	v_pk_mul_f32 v[14:15], v[14:15], v[16:17]
	v_pk_mul_f32 v[16:17], v[22:23], v[18:19] op_sel_hi:[1,0]
	v_pk_mul_f32 v[26:27], v[68:69], v[66:67]
	v_pk_mul_f32 v[8:9], v[8:9], v[16:17]
	v_pk_mul_f32 v[16:17], v[50:51], v[18:19] op_sel_hi:[1,0]
	v_pk_mul_f32 v[8:9], v[24:25], v[8:9]
	v_pk_mul_f32 v[10:11], v[10:11], v[16:17]
	v_pk_mul_f32 v[16:17], v[36:37], v[18:19] op_sel_hi:[1,0]
	v_pk_mul_f32 v[10:11], v[62:63], v[10:11]
	v_pk_mul_f32 v[4:5], v[4:5], v[16:17]
	v_pk_mul_f32 v[16:17], v[54:55], v[18:19] op_sel_hi:[1,0]
	v_pk_mul_f32 v[14:15], v[26:27], v[14:15]
	v_pk_mul_f32 v[6:7], v[6:7], v[16:17]
	v_pk_mul_f32 v[16:17], v[38:39], v[18:19] op_sel_hi:[1,0]
	v_mul_f32_e32 v19, 0xbfb8aa3b, v28
	v_exp_f32_e32 v19, v19
	v_pk_mul_f32 v[0:1], v[0:1], v[16:17]
	v_add_f32_e32 v17, 1.0, v20
	v_rcp_f32_e32 v17, v17
	v_add_f32_e32 v16, 1.0, v19
	v_rcp_f32_e32 v16, v16
	v_pk_mul_f32 v[20:21], v[34:35], v[0:1]
	v_pk_mul_f32 v[0:1], v[30:31], v[18:19] op_sel_hi:[1,0]
	v_pk_mul_f32 v[4:5], v[32:33], v[4:5]
	v_pk_mul_f32 v[0:1], v[2:3], v[0:1]
	v_pk_mul_f32 v[2:3], v[16:17], v[28:29]
	v_pk_mul_f32 v[6:7], v[60:61], v[6:7]
	v_pk_mul_f32 v[16:17], v[2:3], v[0:1]
	v_cvt_pk_bf16_f32 v2, v8, v9
	v_add_u32_e32 v8, 0xc0, v132
	v_ashrrev_i32_e32 v9, 31, v8
	v_lshlrev_b64 v[8:9], 11, v[8:9]
	v_lshl_add_u64 v[8:9], s[0:1], 0, v[8:9]
	v_lshl_add_u64 v[8:9], v[8:9], 0, s[12:13]
	v_lshl_add_u64 v[8:9], v[8:9], 0, v[122:123]
	v_cvt_pk_bf16_f32 v3, v10, v11
	v_lshl_add_u64 v[10:11], v[8:9], 0, s[16:17]
	v_add_co_u32_e32 v8, vcc, s22, v8
	v_cvt_pk_bf16_f32 v0, v12, v13
	v_cvt_pk_bf16_f32 v1, v14, v15
	v_addc_co_u32_e32 v9, vcc, 0, v9, vcc
	v_cvt_pk_bf16_f32 v4, v4, v5
	v_cvt_pk_bf16_f32 v5, v6, v7
	v_cvt_pk_bf16_f32 v6, v20, v21
	v_cvt_pk_bf16_f32 v7, v16, v17
	global_store_dwordx4 v[8:9], v[0:3], off offset:1024
	global_store_dwordx4 v[10:11], v[4:7], off offset:16
	s_barrier
	s_cbranch_scc0 .LBB0_496
